# hgrn_rec: operand images placed in LDS with a chunk-pair swizzle (rows 4..11 of every 16) and matching ds_read_b128 lanes, against 2-way bank conflicts of the 144/272 B pitches
# baseline (speedup 1.0000x reference)
.LBB0_3080:
	s_cmp_gt_i32 s6, 52
	s_cselect_b64 s[0:1], -1, 0
	s_cmp_lt_i32 s7, 53
	s_cselect_b64 s[2:3], -1, 0
	s_or_b64 s[0:1], s[0:1], s[2:3]
	s_and_b64 vcc, exec, s[0:1]
	s_cbranch_vccnz .LBB0_3171
	s_cmpk_gt_i32 s88, 0xff
	s_waitcnt vmcnt(0)
	v_mbcnt_lo_u32_b32 v0, -1, 0
	v_mbcnt_hi_u32_b32 v0, -1, v0
	s_cbranch_scc1 .LBB0_3121
	s_and_b32 s0, s89, 0xffffffc0
	s_add_u32 s18, s94, 0x3d600000
	s_addc_u32 s19, s95, 0
	s_add_u32 s30, s94, 0x47600000
	s_addc_u32 s31, s95, 0
	v_readlane_b32 s24, v253, 20
	s_add_i32 s4, 0, 0x16400
	v_mov_b32_e32 v16, s4
	s_lshl_b32 s4, s24, 3
	v_and_b32_e32 v1, 15, v0
	s_lshl_b32 s16, s24, 4
	s_and_b32 s4, s4, 0x1ffffff0
	v_lshlrev_b32_e32 v3, 3, v0
	s_and_b32 s17, s16, 16
	s_movk_i32 s20, 0x90
	v_or_b32_e32 v93, s4, v1
	v_and_b32_e32 v4, 24, v3
	v_or_b32_e32 v3, s17, v1
	v_mul_lo_u32 v6, v93, s20
	s_movk_i32 s4, 0x110
	v_ashrrev_i32_e32 v7, 2, v0
	s_add_i32 s5, 0, 0x1aa00
	v_add_u32_e32 v2, s0, v0
	v_add_u32_e32 v94, 0, v6
	v_mad_u32_u24 v6, v3, s4, 0
	v_and_b32_e32 v60, -4, v7
	v_mov_b32_e32 v7, s5
	s_add_i32 s5, 0, 0x17600
	s_add_i32 s22, 0, 0x18800
	v_add_u32_e32 v18, 0x18800, v6
	v_mov_b32_e32 v21, s5
	v_add_u32_e32 v24, 0x1aa00, v6
	v_mov_b32_e32 v6, s22
	v_add_u32_e32 v12, 0x800, v2
	v_mad_u32_u24 v17, v3, s20, v16
	v_mad_u32_u24 v95, v3, s4, v7
	v_mad_u32_u24 v22, v3, s20, v21
	v_mad_u32_u24 v96, v3, s4, v6
	v_ashrrev_i32_e32 v3, 31, v2
	v_ashrrev_i32_e32 v13, 31, v12
	s_or_b32 s23, s16, 16
	s_and_b32 s16, s16, 0x3fffffe0
	v_lshrrev_b32_e32 v5, 2, v2
	s_movk_i32 s2, 0xfff
	v_ashrrev_i32_e32 v7, 1, v2
	v_lshlrev_b64 v[62:63], 4, v[2:3]
	v_add_u32_e32 v6, 0x200, v2
	v_add_u32_e32 v8, 0x400, v2
	v_add_u32_e32 v10, 0x600, v2
	v_lshlrev_b64 v[70:71], 4, v[12:13]
	v_or_b32_e32 v3, s23, v1
	v_or_b32_e32 v1, s16, v1
	v_add_u32_e32 v13, s16, v60
	s_add_u32 s33, s94, 0x17600000
	v_bitop3_b32 v89, v5, s2, 63 bitop3:0x6c
	s_movk_i32 s2, 0xfbf
	v_and_b32_e32 v20, -2, v7
	v_ashrrev_i32_e32 v7, 31, v6
	v_ashrrev_i32_e32 v9, 31, v8
	v_ashrrev_i32_e32 v11, 31, v10
	v_add_u32_e32 v14, 0xa00, v2
	v_mul_lo_u32 v3, v3, s20
	v_mul_lo_u32 v1, v1, s20
	v_lshlrev_b32_e32 v97, 2, v13
	v_lshlrev_b32_e32 v98, 1, v13
	v_add_u32_e32 v13, s23, v60
	s_addc_u32 s34, s95, 0
	s_lshl_b32 s16, s24, 8
	s_movk_i32 s0, 0x1100
	v_bfe_u32 v88, v2, 2, 6
	v_mov_b32_e32 v57, 0
	v_bitop3_b32 v90, v5, s2, 63 bitop3:0x6c
	s_movk_i32 s2, 0x100
	v_lshlrev_b32_e32 v56, 1, v4
	v_and_b32_e32 v92, -16, v0
	v_lshl_add_u32 v19, v93, 7, v94
	v_add_u32_e32 v23, 0xb200, v94
	v_lshlrev_b64 v[64:65], 4, v[6:7]
	v_lshlrev_b64 v[66:67], 4, v[8:9]
	v_lshlrev_b64 v[68:69], 4, v[10:11]
	v_ashrrev_i32_e32 v15, 31, v14
	v_add_u32_e32 v3, 0, v3
	s_movk_i32 s4, 0xb20
	v_lshlrev_b32_e32 v7, 4, v2
	s_movk_i32 s6, 0x920
	v_lshlrev_b32_e32 v6, 4, v6
	s_movk_i32 s8, 0x720
	v_lshlrev_b32_e32 v8, 4, v8
	s_movk_i32 s10, 0x520
	v_lshlrev_b32_e32 v9, 4, v10
	s_movk_i32 s12, 0x320
	v_lshlrev_b32_e32 v10, 4, v12
	s_movk_i32 s14, 0x120
	v_lshlrev_b32_e32 v11, 4, v14
	v_mad_u32_u24 v12, v4, s20, v16
	v_add_u32_e32 v1, 0, v1
	v_lshlrev_b32_e32 v99, 2, v13
	v_lshlrev_b32_e32 v100, 1, v13
	v_mad_u32_u24 v13, v4, s20, v21
	s_add_i32 s22, s22, s16
	s_movk_i32 s16, 0xf3f
	v_cmp_gt_i32_e64 s[0:1], s0, v2
	s_mov_b32 s21, 0
	v_or_b32_e32 v91, 64, v88
	v_cmp_gt_i32_e64 s[2:3], s2, v2
	v_lshl_add_u64 v[58:59], s[18:19], 0, v[56:57]
	v_ashrrev_i32_e32 v61, 31, v60
	v_lshlrev_b64 v[72:73], 4, v[14:15]
	v_cmp_gt_i32_e64 s[4:5], s4, v2
	v_cmp_gt_i32_e64 s[6:7], s6, v2
	v_cmp_gt_i32_e64 s[8:9], s8, v2
	v_cmp_gt_i32_e64 s[10:11], s10, v2
	v_cmp_gt_i32_e64 s[12:13], s12, v2
	v_cmp_gt_i32_e64 s[14:15], s14, v2
	v_add_u32_e32 v101, 0xfffffe00, v2
	v_lshl_add_u32 v102, v0, 2, s22
	v_bitop3_b32 v103, v5, s16, 63 bitop3:0x6c
	v_sub_u32_e32 v104, 0xfbf, v93
	s_movk_i32 s35, 0xeff
	s_movk_i32 s36, 0x2800
	v_lshlrev_b32_e32 v74, 1, v4
	s_lshl_b32 s37, s17, 2
	v_lshrrev_b32_e32 v201, 2, v0
	v_lshrrev_b32_e32 v202, 3, v0
	v_xor_b32_e32 v201, v201, v202
	v_and_b32_e32 v201, 1, v201
	v_lshrrev_b32_e32 v202, 4, v0
	v_xor_b32_e32 v201, v201, v202
	v_lshlrev_b32_e32 v200, 4, v201
	v_add_u32_e32 v105, v12, v20
	v_add_u32_e32 v106, v17, v92
	v_add_u32_e32 v107, v18, v92
	v_add_u32_e32 v108, v19, v200
	v_add_u32_e32 v109, v13, v20
	v_add_u32_e32 v110, v22, v92
	v_add_u32_e32 v111, v23, v200
	v_add_u32_e32 v112, v24, v92
	s_add_i32 s38, 0, 0x16200
	v_mov_b32_e32 v113, 0x2800
	v_add_u32_e32 v114, 0, v7
	v_add_u32_e32 v115, 0, v6
	v_add_u32_e32 v116, 0, v8
	v_add_u32_e32 v117, 0, v9
	v_add_u32_e32 v118, 0, v10
	v_add_u32_e32 v119, 0, v11
	v_mov_b32_e32 v207, 0xf10
	v_mov_b32_e32 v208, 0x1c72
	v_mov_b32_e32 v209, 17
	v_mov_b32_e32 v210, 9
	v_mov_b32_e32 v211, 16
	v_mov_b32_e32 v212, 8
	v_mov_b32_e32 v201, v2
	v_add_u32_e32 v202, 0xfffffbc0, v201
	v_cmp_gt_u32_e32 vcc, 0x440, v201
	v_cndmask_b32_e32 v202, v202, v201, vcc
	v_cndmask_b32_e32 v203, v208, v207, vcc
	v_cndmask_b32_e32 v204, v210, v209, vcc
	v_cndmask_b32_e32 v213, v212, v211, vcc
	v_mul_lo_u32 v205, v202, v203
	v_lshrrev_b32_e32 v205, 16, v205
	v_mul_lo_u32 v206, v205, v204
	v_sub_u32_e32 v206, v202, v206
	v_lshrrev_b32_e32 v203, 2, v205
	v_lshrrev_b32_e32 v204, 3, v205
	v_xor_b32_e32 v203, v203, v204
	v_and_b32_e32 v203, 1, v203
	v_cmp_lt_u32_e32 vcc, v206, v213
	v_cndmask_b32_e32 v203, 0, v203, vcc
	v_cmp_gt_u32_e32 vcc, 0xb00, v201
	v_cndmask_b32_e32 v203, 0, v203, vcc
	v_and_b32_e32 v204, 1, v206
	v_lshlrev_b32_e32 v204, 1, v204
	v_sub_u32_e32 v204, 1, v204
	v_mul_lo_u32 v204, v204, v203
	v_add_u32_e32 v201, v201, v204
	v_lshlrev_b32_e32 v114, 4, v201
	v_add_u32_e32 v201, 512, v2
	v_add_u32_e32 v202, 0xfffffbc0, v201
	v_cmp_gt_u32_e32 vcc, 0x440, v201
	v_cndmask_b32_e32 v202, v202, v201, vcc
	v_cndmask_b32_e32 v203, v208, v207, vcc
	v_cndmask_b32_e32 v204, v210, v209, vcc
	v_cndmask_b32_e32 v213, v212, v211, vcc
	v_mul_lo_u32 v205, v202, v203
	v_lshrrev_b32_e32 v205, 16, v205
	v_mul_lo_u32 v206, v205, v204
	v_sub_u32_e32 v206, v202, v206
	v_lshrrev_b32_e32 v203, 2, v205
	v_lshrrev_b32_e32 v204, 3, v205
	v_xor_b32_e32 v203, v203, v204
	v_and_b32_e32 v203, 1, v203
	v_cmp_lt_u32_e32 vcc, v206, v213
	v_cndmask_b32_e32 v203, 0, v203, vcc
	v_cmp_gt_u32_e32 vcc, 0xb00, v201
	v_cndmask_b32_e32 v203, 0, v203, vcc
	v_and_b32_e32 v204, 1, v206
	v_lshlrev_b32_e32 v204, 1, v204
	v_sub_u32_e32 v204, 1, v204
	v_mul_lo_u32 v204, v204, v203
	v_add_u32_e32 v201, v201, v204
	v_lshlrev_b32_e32 v115, 4, v201
	v_add_u32_e32 v201, 1024, v2
	v_add_u32_e32 v202, 0xfffffbc0, v201
	v_cmp_gt_u32_e32 vcc, 0x440, v201
	v_cndmask_b32_e32 v202, v202, v201, vcc
	v_cndmask_b32_e32 v203, v208, v207, vcc
	v_cndmask_b32_e32 v204, v210, v209, vcc
	v_cndmask_b32_e32 v213, v212, v211, vcc
	v_mul_lo_u32 v205, v202, v203
	v_lshrrev_b32_e32 v205, 16, v205
	v_mul_lo_u32 v206, v205, v204
	v_sub_u32_e32 v206, v202, v206
	v_lshrrev_b32_e32 v203, 2, v205
	v_lshrrev_b32_e32 v204, 3, v205
	v_xor_b32_e32 v203, v203, v204
	v_and_b32_e32 v203, 1, v203
	v_cmp_lt_u32_e32 vcc, v206, v213
	v_cndmask_b32_e32 v203, 0, v203, vcc
	v_cmp_gt_u32_e32 vcc, 0xb00, v201
	v_cndmask_b32_e32 v203, 0, v203, vcc
	v_and_b32_e32 v204, 1, v206
	v_lshlrev_b32_e32 v204, 1, v204
	v_sub_u32_e32 v204, 1, v204
	v_mul_lo_u32 v204, v204, v203
	v_add_u32_e32 v201, v201, v204
	v_lshlrev_b32_e32 v116, 4, v201
	v_add_u32_e32 v201, 1536, v2
	v_add_u32_e32 v202, 0xfffffbc0, v201
	v_cmp_gt_u32_e32 vcc, 0x440, v201
	v_cndmask_b32_e32 v202, v202, v201, vcc
	v_cndmask_b32_e32 v203, v208, v207, vcc
	v_cndmask_b32_e32 v204, v210, v209, vcc
	v_cndmask_b32_e32 v213, v212, v211, vcc
	v_mul_lo_u32 v205, v202, v203
	v_lshrrev_b32_e32 v205, 16, v205
	v_mul_lo_u32 v206, v205, v204
	v_sub_u32_e32 v206, v202, v206
	v_lshrrev_b32_e32 v203, 2, v205
	v_lshrrev_b32_e32 v204, 3, v205
	v_xor_b32_e32 v203, v203, v204
	v_and_b32_e32 v203, 1, v203
	v_cmp_lt_u32_e32 vcc, v206, v213
	v_cndmask_b32_e32 v203, 0, v203, vcc
	v_cmp_gt_u32_e32 vcc, 0xb00, v201
	v_cndmask_b32_e32 v203, 0, v203, vcc
	v_and_b32_e32 v204, 1, v206
	v_lshlrev_b32_e32 v204, 1, v204
	v_sub_u32_e32 v204, 1, v204
	v_mul_lo_u32 v204, v204, v203
	v_add_u32_e32 v201, v201, v204
	v_lshlrev_b32_e32 v117, 4, v201
	v_add_u32_e32 v201, 2048, v2
	v_add_u32_e32 v202, 0xfffffbc0, v201
	v_cmp_gt_u32_e32 vcc, 0x440, v201
	v_cndmask_b32_e32 v202, v202, v201, vcc
	v_cndmask_b32_e32 v203, v208, v207, vcc
	v_cndmask_b32_e32 v204, v210, v209, vcc
	v_cndmask_b32_e32 v213, v212, v211, vcc
	v_mul_lo_u32 v205, v202, v203
	v_lshrrev_b32_e32 v205, 16, v205
	v_mul_lo_u32 v206, v205, v204
	v_sub_u32_e32 v206, v202, v206
	v_lshrrev_b32_e32 v203, 2, v205
	v_lshrrev_b32_e32 v204, 3, v205
	v_xor_b32_e32 v203, v203, v204
	v_and_b32_e32 v203, 1, v203
	v_cmp_lt_u32_e32 vcc, v206, v213
	v_cndmask_b32_e32 v203, 0, v203, vcc
	v_cmp_gt_u32_e32 vcc, 0xb00, v201
	v_cndmask_b32_e32 v203, 0, v203, vcc
	v_and_b32_e32 v204, 1, v206
	v_lshlrev_b32_e32 v204, 1, v204
	v_sub_u32_e32 v204, 1, v204
	v_mul_lo_u32 v204, v204, v203
	v_add_u32_e32 v201, v201, v204
	v_lshlrev_b32_e32 v118, 4, v201
	v_add_u32_e32 v201, 2560, v2
	v_add_u32_e32 v202, 0xfffffbc0, v201
	v_cmp_gt_u32_e32 vcc, 0x440, v201
	v_cndmask_b32_e32 v202, v202, v201, vcc
	v_cndmask_b32_e32 v203, v208, v207, vcc
	v_cndmask_b32_e32 v204, v210, v209, vcc
	v_cndmask_b32_e32 v213, v212, v211, vcc
	v_mul_lo_u32 v205, v202, v203
	v_lshrrev_b32_e32 v205, 16, v205
	v_mul_lo_u32 v206, v205, v204
	v_sub_u32_e32 v206, v202, v206
	v_lshrrev_b32_e32 v203, 2, v205
	v_lshrrev_b32_e32 v204, 3, v205
	v_xor_b32_e32 v203, v203, v204
	v_and_b32_e32 v203, 1, v203
	v_cmp_lt_u32_e32 vcc, v206, v213
	v_cndmask_b32_e32 v203, 0, v203, vcc
	v_cmp_gt_u32_e32 vcc, 0xb00, v201
	v_cndmask_b32_e32 v203, 0, v203, vcc
	v_and_b32_e32 v204, 1, v206
	v_lshlrev_b32_e32 v204, 1, v204
	v_sub_u32_e32 v204, 1, v204
	v_mul_lo_u32 v204, v204, v203
	v_add_u32_e32 v201, v201, v204
	v_lshlrev_b32_e32 v119, 4, v201
	v_add_u32_e32 v120, v1, v200
	v_add_u32_e32 v121, v3, v200
	s_mov_b32 s39, s88
	s_branch .LBB0_3084

.LBB0_3099:
	ds_read_b128 v[124:127], v106
	v_add_u32_e32 v56, v94, v200
	ds_read_b128 v[128:131], v56 offset:35840
	ds_read_b128 v[132:135], v106 offset:64
	ds_read_b128 v[136:139], v56 offset:35904
	ds_read_b128 v[140:143], v120 offset:17408
	ds_read_b128 v[144:147], v120 offset:17472
	v_add_u32_e32 v56, 64, v75
	s_waitcnt lgkmcnt(1)
	v_mfma_f32_16x16x32_bf16 v[140:143], v[140:143], v[124:127], 0
	v_mfma_f32_16x16x32_bf16 v[128:131], v[124:127], v[128:131], 0
	ds_read_b128 v[124:127], v107
	ds_read_b128 v[148:151], v108
	ds_read_b128 v[152:155], v107 offset:64
	v_mfma_f32_16x16x32_bf16 v[128:131], v[132:135], v[136:139], v[128:131]
	ds_read_b128 v[136:139], v108 offset:64
	ds_read_b128 v[156:159], v107 offset:128
	ds_read_b128 v[160:163], v107 offset:192
	s_waitcnt lgkmcnt(4)
	v_mfma_f32_16x16x32_bf16 v[126:129], v[124:127], v[148:151], v[128:131]
	ds_read_b128 v[148:151], v108 offset:128
	ds_read_b128 v[164:167], v108 offset:192
	v_add_u32_e32 v124, s40, v93
	v_cndmask_b32_e64 v130, v56, v124, s[16:17]
	s_waitcnt lgkmcnt(4)
	v_mfma_f32_16x16x32_bf16 v[126:129], v[152:155], v[136:139], v[126:129]
	v_add_u32_e32 v56, 0, v97
	v_ashrrev_i32_e32 v131, 31, v130
	ds_read_b128 v[136:139], v56 offset:45056
	s_waitcnt lgkmcnt(2)
	v_mfma_f32_16x16x32_bf16 v[126:129], v[156:159], v[148:151], v[126:129]
	v_lshl_add_u64 v[148:149], s[24:25], 0, v[130:131]
	v_add_u32_e32 v56, v95, v98
	v_mfma_f32_16x16x32_bf16 v[130:133], v[144:147], v[132:135], v[140:143]
	v_lshlrev_b64 v[134:135], 12, v[148:149]
	v_lshl_add_u64 v[134:135], v[78:79], 0, v[134:135]
	s_waitcnt lgkmcnt(1)
	v_mfma_f32_16x16x32_bf16 v[126:129], v[160:163], v[164:167], v[126:129]
	s_waitcnt lgkmcnt(0)
	s_nop 2
	v_pk_fma_f32 v[82:83], v[82:83], v[138:139], v[132:133]
	s_nop 2
	global_store_dwordx4 v[134:135], v[126:129], off
	v_pk_fma_f32 v[80:81], v[80:81], v[136:137], v[130:131]
	s_nop 0
	v_cvt_pk_bf16_f32 v126, v80, v81
	v_cvt_pk_bf16_f32 v127, v82, v83
	ds_write_b64 v56, v[126:127]
	ds_read_b128 v[126:129], v121 offset:17408
	ds_read_b128 v[130:133], v121 offset:17472
	ds_read_b128 v[134:137], v106
	ds_read_b128 v[138:141], v106 offset:64
	s_waitcnt lgkmcnt(1)
	v_mfma_f32_16x16x32_bf16 v[126:129], v[126:129], v[134:137], 0
	v_add_u32_e32 v56, 0, v99
	ds_read_b128 v[134:137], v56 offset:45056
	v_add_u32_e32 v56, v95, v100
	s_waitcnt lgkmcnt(1)
	v_mfma_f32_16x16x32_bf16 v[126:129], v[130:133], v[138:141], v[126:129]
	s_waitcnt lgkmcnt(0)
	s_nop 6
	v_pk_fma_f32 v[86:87], v[86:87], v[136:137], v[128:129]
	v_pk_fma_f32 v[84:85], v[84:85], v[134:135], v[126:127]
	s_nop 0
	v_cvt_pk_bf16_f32 v126, v84, v85
	v_cvt_pk_bf16_f32 v127, v86, v87
	ds_write_b64 v56, v[126:127]
	s_and_saveexec_b64 s[28:29], s[4:5]
	s_cbranch_execz .LBB0_3115
	s_waitcnt vmcnt(7)
	ds_write_b128 v114, v[24:27] offset:45568
	s_or_b64 exec, exec, s[28:29]
	s_and_saveexec_b64 s[28:29], s[6:7]
	s_cbranch_execnz .LBB0_3116
